# proj V variant: removed six small global loads (Wka fragments, bka) that the V path never uses and that sat ahead of its main tile loads
# speedup vs baseline: 1.0181x; 1.0159x over previous
_Z11proj_kernelPKfS0_S0_S0_S0_S0_S0_S0_S0_S0_S0_S0_S0_PfS1_PDF16_S1_S0_S0_S2_:
	s_load_dwordx2 s[16:17], s[0:1], 0x90
	s_load_dwordx4 s[4:7], s[0:1], 0x80
	s_cmpk_gt_u32 s2, 0x5f
	s_mov_b64 s[8:9], -1
	s_cbranch_scc0 .LBB0_16
	s_load_dwordx4 s[8:11], s[0:1], 0x58
	s_lshr_b32 s3, s2, 3
	s_cmpk_gt_u32 s2, 0xbf
	s_mov_b64 s[12:13], -1
	s_cbranch_scc0 .LBB0_3
	v_lshlrev_b32_e32 v54, 2, v0
	v_mov_b32_e32 v55, 0
	s_waitcnt lgkmcnt(0)
	v_lshl_add_u64 v[2:3], s[6:7], 0, v[54:55]
	v_lshl_add_u64 v[4:5], s[16:17], 0, v[54:55]
	v_cmp_gt_u32_e32 vcc, 64, v0
	s_load_dwordx4 s[12:15], s[0:1], 0x38
	s_load_dwordx2 s[22:23], s[0:1], 0x10
	v_cndmask_b32_e32 v2, v4, v2, vcc
	v_cndmask_b32_e32 v3, v5, v3, vcc
	global_load_dword v70, v[2:3], off
	v_lshrrev_b32_e32 v2, 2, v0
	v_and_b32_e32 v56, 15, v0
	v_and_b32_e32 v18, 48, v2
	v_or_b32_e32 v68, v18, v56
	v_bfe_u32 v1, v0, 4, 2
	v_lshlrev_b32_e32 v2, 8, v68
	v_mov_b32_e32 v3, v55
	s_lshl_b32 s20, s2, 1
	v_lshl_add_u64 v[2:3], s[8:9], 0, v[2:3]
	v_lshlrev_b32_e32 v4, 5, v1
	v_mov_b32_e32 v5, v55
	s_and_b32 s20, s20, 6
	s_bfe_u32 s21, s2, 0x10003
	v_lshl_add_u64 v[14:15], v[2:3], 0, v[4:5]
	s_sub_i32 s19, s3, 24
	s_or_b32 s21, s21, s20
	v_lshl_add_u64 v[6:7], v[14:15], 0, 16
	s_mov_b64 s[24:25], 0x80
	s_bfe_u32 s18, s2, 0x10002
	s_lshr_b32 s19, s19, 1
	s_lshl_b32 s20, s21, 6
	v_lshl_add_u64 v[10:11], v[14:15], 0, s[24:25]
	s_mov_b64 s[24:25], 0x90
	v_lshlrev_b32_e32 v22, 2, v18
	v_mov_b32_e32 v23, v55
	s_lshl_b32 s21, s21, 8
	v_lshl_add_u64 v[14:15], v[14:15], 0, s[24:25]
	v_lshl_add_u64 v[24:25], s[10:11], 0, v[22:23]
	v_lshlrev_b32_e32 v18, 4, v1
	v_mov_b32_e32 v19, v55
	s_waitcnt lgkmcnt(0)
	s_add_u32 s14, s14, s21
	v_lshl_add_u64 v[18:19], v[24:25], 0, v[18:19]
	s_addc_u32 s15, s15, 0
	v_lshlrev_b32_e32 v26, 2, v56
	v_mov_b32_e32 v27, v55
	v_lshl_add_u64 v[22:23], s[14:15], 0, v[22:23]
	s_mul_i32 s26, s18, 0x180
	v_lshrrev_b32_e32 v57, 4, v0
	v_lshl_add_u64 v[24:25], v[24:25], 0, v[26:27]
	v_lshl_add_u64 v[22:23], v[22:23], 0, v[26:27]
	s_mulk_i32 s19, 0x60
	global_load_dword v69, v[22:23], off
	v_or_b32_e32 v22, s26, v57
	v_add_u32_e32 v22, s19, v22
	v_mov_b32_e32 v23, v55
	v_lshlrev_b64 v[22:23], 11, v[22:23]
	v_and_b32_e32 v72, 60, v54
	v_lshl_add_u64 v[22:23], s[22:23], 0, v[22:23]
	v_lshlrev_b32_e32 v54, 2, v72
	v_lshl_add_u64 v[66:67], v[22:23], 0, v[54:55]
	global_load_dwordx4 v[22:25], v[66:67], off
	s_mov_b32 s14, 0x10000
	v_add_co_u32_e32 v64, vcc, s14, v66
	s_mov_b32 s15, 0x20000
	s_nop 0
	v_addc_co_u32_e32 v65, vcc, 0, v67, vcc
	global_load_dwordx4 v[30:33], v[64:65], off
	v_add_co_u32_e32 v62, vcc, s15, v66
	v_or_b32_e32 v26, s20, v57
	s_nop 0
	v_addc_co_u32_e32 v63, vcc, 0, v67, vcc
	global_load_dwordx4 v[34:37], v[62:63], off
	v_lshlrev_b32_e32 v26, 9, v26
	v_lshl_add_u64 v[26:27], v[26:27], 2, s[12:13]
	v_lshl_add_u64 v[60:61], v[26:27], 0, v[54:55]
	v_add_co_u32_e32 v58, vcc, s14, v60
	global_load_dwordx4 v[38:41], v[60:61], off
	s_nop 0
	v_addc_co_u32_e32 v59, vcc, 0, v61, vcc
	global_load_dwordx4 v[42:45], v[58:59], off
	global_load_dwordx4 v[46:49], v[66:67], off offset:256
	global_load_dwordx4 v[50:53], v[64:65], off offset:256
	global_load_dwordx4 v[74:77], v[62:63], off offset:256
	global_load_dwordx4 v[78:81], v[60:61], off offset:256
	global_load_dwordx4 v[82:85], v[58:59], off offset:256
	global_load_dwordx4 v[86:89], v[66:67], off offset:512
	global_load_dwordx4 v[90:93], v[64:65], off offset:512
	v_lshrrev_b32_e32 v26, 8, v0
	v_mul_u32_u24_e32 v54, 48, v26
	global_load_dwordx4 v[26:29], v[62:63], off offset:512
	global_load_dwordx4 v[94:97], v[60:61], off offset:512
	v_or_b32_e32 v102, v54, v56
	v_and_b32_e32 v56, 48, v0
	s_movk_i32 s14, 0x90
	v_mad_u32_u24 v73, v68, s14, v56
	v_lshl_or_b32 v1, v1, 2, v54
	v_mul_lo_u32 v1, v1, s14
	v_lshl_add_u32 v1, v68, 1, v1
	s_movk_i32 s15, 0x180
	s_waitcnt vmcnt(13)
	v_cvt_f16_f32_e32 v22, v22
	v_cvt_f16_f32_e32 v25, v25
	v_cvt_pk_f16_f32 v23, v23, v24
	v_mul_u32_u24_e32 v24, 0x90, v57
	v_pack_b32_f16 v22, v22, v23
	v_alignbit_b32 v23, v25, v23, 16
	v_lshl_add_u32 v72, v72, 1, v24
	s_waitcnt vmcnt(12)
	v_cvt_f16_f32_e32 v25, v30
	v_cvt_f16_f32_e32 v30, v33
	v_cvt_pk_f16_f32 v31, v31, v32
	v_mad_u64_u32 v[56:57], s[12:13], v102, s14, v[56:57]
	v_pack_b32_f16 v24, v25, v31
	v_alignbit_b32 v25, v30, v31, 16
	s_waitcnt vmcnt(11)
	v_cvt_f16_f32_e32 v30, v34
	ds_write2st64_b64 v72, v[22:23], v[24:25] offset1:9
	s_waitcnt vmcnt(8)
	v_cvt_f16_f32_e32 v34, v46
	v_cvt_pk_f16_f32 v23, v35, v36
	v_cvt_f16_f32_e32 v35, v49
	v_cvt_pk_f16_f32 v36, v47, v48
	v_pack_b32_f16 v102, v34, v36
	s_waitcnt vmcnt(7)
	v_cvt_f16_f32_e32 v34, v50
	v_alignbit_b32 v103, v35, v36, 16
	v_cvt_f16_f32_e32 v35, v53
	v_cvt_pk_f16_f32 v36, v51, v52
	v_pack_b32_f16 v104, v34, v36
	s_waitcnt vmcnt(6)
	v_cvt_f16_f32_e32 v34, v74
	v_alignbit_b32 v105, v35, v36, 16
	v_cvt_f16_f32_e32 v35, v77
	v_cvt_pk_f16_f32 v36, v75, v76
	v_pack_b32_f16 v106, v34, v36
	s_waitcnt vmcnt(5)
	v_cvt_f16_f32_e32 v34, v78
	v_alignbit_b32 v107, v35, v36, 16
	v_cvt_f16_f32_e32 v35, v81
	v_cvt_pk_f16_f32 v36, v79, v80
	v_pack_b32_f16 v108, v34, v36
	s_waitcnt vmcnt(4)
	v_cvt_f16_f32_e32 v34, v82
	v_cvt_f16_f32_e32 v24, v37
	v_pack_b32_f16 v22, v30, v23
	v_cvt_f16_f32_e32 v25, v38
	v_cvt_f16_f32_e32 v30, v41
	v_alignbit_b32 v109, v35, v36, 16
	v_cvt_f16_f32_e32 v35, v85
	v_cvt_pk_f16_f32 v36, v83, v84
	v_cvt_pk_f16_f32 v31, v39, v40
	v_pack_b32_f16 v110, v34, v36
	s_waitcnt vmcnt(3)
	v_cvt_f16_f32_e32 v34, v86
	v_alignbit_b32 v23, v24, v23, 16
	v_pack_b32_f16 v24, v25, v31
	v_alignbit_b32 v25, v30, v31, 16
	v_cvt_f16_f32_e32 v30, v42
	v_cvt_f16_f32_e32 v31, v45
	v_alignbit_b32 v111, v35, v36, 16
	v_cvt_pk_f16_f32 v36, v87, v88
	v_cvt_pk_f16_f32 v32, v43, v44
	v_cvt_f16_f32_e32 v35, v89
	v_pack_b32_f16 v114, v34, v36
	s_waitcnt vmcnt(2)
	v_cvt_f16_f32_e32 v34, v90
	v_pack_b32_f16 v30, v30, v32
	v_alignbit_b32 v31, v31, v32, 16
	ds_write2st64_b64 v72, v[22:23], v[24:25] offset0:18 offset1:54
	global_load_dwordx4 v[22:25], v[58:59], off offset:512
	ds_write_b64 v72, v[30:31] offset:32256
	s_waitcnt lgkmcnt(0)
	s_barrier
	global_load_dwordx4 v[30:33], v[66:67], off offset:768
	global_load_dwordx4 v[98:101], v[64:65], off offset:768
	v_cvt_pk_f16_f32 v39, v91, v92
	v_alignbit_b32 v115, v35, v36, 16
	v_cvt_f16_f32_e32 v38, v93
	v_pack_b32_f16 v116, v34, v39
	ds_read_b128 v[34:37], v56
	s_waitcnt vmcnt(4)
	v_cvt_f16_f32_e32 v57, v26
	v_alignbit_b32 v117, v38, v39, 16
	ds_read_b128 v[38:41], v56 offset:2304
	ds_read_b128 v[46:49], v73 offset:27648
	ds_read_b128 v[50:53], v56 offset:4608
	ds_read_b128 v[74:77], v56 offset:64
	ds_read_b128 v[78:81], v73 offset:27712
	v_cvt_f16_f32_e32 v87, v29
	s_waitcnt lgkmcnt(3)
	v_mfma_f32_16x16x32_f16 v[34:37], v[34:37], v[46:49], 0
	v_cvt_pk_f16_f32 v86, v27, v28
	global_load_dwordx4 v[42:45], v[62:63], off offset:768
	ds_read_b128 v[26:29], v56 offset:2368
	v_mfma_f32_16x16x32_f16 v[82:85], v[38:41], v[46:49], 0
	v_pack_b32_f16 v118, v57, v86
	v_alignbit_b32 v119, v87, v86, 16
	ds_read_b128 v[86:89], v56 offset:4672
	s_waitcnt lgkmcnt(4)
	v_mfma_f32_16x16x32_f16 v[50:53], v[50:53], v[46:49], 0
	global_load_dwordx4 v[46:49], v[60:61], off offset:768
	ds_write2st64_b64 v72, v[102:103], v[104:105] offset0:27 offset1:36
	ds_write2st64_b64 v72, v[106:107], v[108:109] offset0:45 offset1:72
	ds_write_b64 v72, v[110:111] offset:41472
	s_waitcnt lgkmcnt(5)
	v_mfma_f32_16x16x32_f16 v[74:77], v[74:77], v[78:81], v[34:37]
	s_waitcnt vmcnt(5)
	v_cvt_f16_f32_e32 v57, v94
	v_cvt_f16_f32_e32 v90, v97
	v_cvt_pk_f16_f32 v91, v95, v96
	global_load_dwordx4 v[34:37], v[58:59], off offset:768
	s_waitcnt lgkmcnt(0)
	s_barrier
	global_load_dwordx4 v[38:41], v[66:67], off offset:1024
	v_pack_b32_f16 v120, v57, v91
	v_alignbit_b32 v121, v90, v91, 16
	global_load_dwordx4 v[90:93], v[64:65], off offset:1024
	v_mfma_f32_16x16x32_f16 v[50:53], v[86:89], v[78:81], v[50:53]
	global_load_dwordx4 v[86:89], v[62:63], off offset:1024
	s_load_dwordx2 s[12:13], s[0:1], 0x78
	s_waitcnt vmcnt(8)
	v_cvt_f16_f32_e32 v22, v22
	v_mfma_f32_16x16x32_f16 v[82:85], v[26:29], v[78:81], v[82:85]
	v_cvt_f16_f32_e32 v25, v25
	v_cvt_pk_f16_f32 v23, v23, v24
	v_pack_b32_f16 v122, v22, v23
	s_waitcnt vmcnt(7)
	v_cvt_f16_f32_e32 v26, v30
	v_cvt_pk_f16_f32 v57, v31, v32
	v_alignbit_b32 v123, v25, v23, 16
	ds_read_b128 v[22:25], v56 offset:13824
	ds_read_b128 v[78:81], v73 offset:36864
	v_cvt_f16_f32_e32 v125, v33
	s_waitcnt vmcnt(6)
	v_cvt_f16_f32_e32 v126, v98
	v_cvt_pk_f16_f32 v127, v99, v100
	v_cvt_f16_f32_e32 v128, v101
	ds_read_b128 v[94:97], v56 offset:13888
	ds_read_b128 v[98:101], v73 offset:36928
	ds_read_b128 v[30:33], v56 offset:16128
	ds_read_b128 v[102:105], v56 offset:16192
	ds_read_b128 v[106:109], v56 offset:18432
	ds_read_b128 v[110:113], v56 offset:18496
	ds_write2st64_b64 v72, v[114:115], v[116:117] offset1:9
	global_load_dwordx4 v[114:117], v[60:61], off offset:1024
	v_pack_b32_f16 v124, v26, v57
	global_load_dwordx4 v[26:29], v[58:59], off offset:1024
	s_waitcnt lgkmcnt(0)
	v_mfma_f32_16x16x32_f16 v[74:77], v[22:25], v[78:81], v[74:77]
	ds_write2st64_b64 v72, v[118:119], v[120:121] offset0:18 offset1:54
	s_waitcnt vmcnt(7)
	v_cvt_f16_f32_e32 v42, v42
	v_cvt_f16_f32_e32 v45, v45
	v_mfma_f32_16x16x32_f16 v[82:85], v[30:33], v[78:81], v[82:85]
	ds_write_b64 v72, v[122:123] offset:32256
	s_waitcnt lgkmcnt(0)
	s_barrier
	global_load_dwordx4 v[22:25], v[66:67], off offset:1280
	global_load_dwordx4 v[30:33], v[64:65], off offset:1280
	v_cvt_pk_f16_f32 v43, v43, v44
	v_alignbit_b32 v125, v125, v57, 16
	v_mfma_f32_16x16x32_f16 v[50:53], v[106:109], v[78:81], v[50:53]
	v_pack_b32_f16 v108, v42, v43
	v_alignbit_b32 v109, v45, v43, 16
	s_waitcnt vmcnt(7)
	v_cvt_f16_f32_e32 v34, v34
	v_cvt_pk_f16_f32 v35, v35, v36
	v_cvt_f16_f32_e32 v36, v37
	v_mfma_f32_16x16x32_f16 v[42:45], v[94:97], v[98:101], v[74:77]
	v_cvt_f16_f32_e32 v57, v46
	s_waitcnt vmcnt(6)
	v_cvt_f16_f32_e32 v37, v41
	v_pack_b32_f16 v106, v126, v127
	v_cvt_f16_f32_e32 v74, v49
	v_cvt_pk_f16_f32 v75, v47, v48
	v_mfma_f32_16x16x32_f16 v[46:49], v[102:105], v[98:101], v[82:85]
	v_pack_b32_f16 v104, v34, v35
	v_cvt_f16_f32_e32 v34, v38
	v_alignbit_b32 v105, v36, v35, 16
	v_cvt_pk_f16_f32 v35, v39, v40
	v_alignbit_b32 v119, v37, v35, 16
	v_pack_b32_f16 v118, v34, v35
	ds_read_b128 v[34:37], v56
	v_pack_b32_f16 v102, v57, v75
	v_alignbit_b32 v103, v74, v75, 16
	ds_read_b128 v[74:77], v56 offset:2304
	ds_read_b128 v[78:81], v73 offset:27648
	s_waitcnt vmcnt(5)
	v_cvt_f16_f32_e32 v38, v90
	v_cvt_f16_f32_e32 v40, v93
	v_mfma_f32_16x16x32_f16 v[50:53], v[110:113], v[98:101], v[50:53]
	v_cvt_pk_f16_f32 v39, v91, v92
	v_pack_b32_f16 v120, v38, v39
	v_alignbit_b32 v121, v40, v39, 16
	ds_read_b128 v[82:85], v56 offset:4608
	ds_read_b128 v[90:93], v56 offset:64
	ds_read_b128 v[94:97], v73 offset:27712
	s_waitcnt lgkmcnt(3)
	v_mfma_f32_16x16x32_f16 v[34:37], v[34:37], v[78:81], v[42:45]
	global_load_dwordx4 v[38:41], v[62:63], off offset:1280
	v_alignbit_b32 v107, v128, v127, 16
	ds_read_b128 v[98:101], v56 offset:2368
	s_waitcnt vmcnt(5)
	v_cvt_f16_f32_e32 v42, v86
	v_cvt_f16_f32_e32 v44, v89
	v_mfma_f32_16x16x32_f16 v[74:77], v[74:77], v[78:81], v[46:49]
	v_cvt_pk_f16_f32 v43, v87, v88
	v_pack_b32_f16 v122, v42, v43
	v_alignbit_b32 v123, v44, v43, 16
	s_waitcnt lgkmcnt(3)
	v_mfma_f32_16x16x32_f16 v[78:81], v[82:85], v[78:81], v[50:53]
	global_load_dwordx4 v[42:45], v[58:59], off offset:1280
	ds_read_b128 v[86:89], v56 offset:4672
	ds_write2st64_b64 v72, v[124:125], v[106:107] offset0:27 offset1:36
	global_load_dwordx4 v[50:53], v[60:61], off offset:1280
	ds_write2st64_b64 v72, v[108:109], v[102:103] offset0:45 offset1:72
	ds_write_b64 v72, v[104:105] offset:41472
	s_waitcnt lgkmcnt(0)
	s_barrier
	global_load_dwordx4 v[46:49], v[66:67], off offset:1536
	global_load_dwordx4 v[82:85], v[64:65], off offset:1536
	v_mfma_f32_16x16x32_f16 v[78:81], v[86:89], v[94:97], v[78:81]
	ds_read_b128 v[86:89], v73 offset:36864
	s_waitcnt vmcnt(8)
	v_cvt_f16_f32_e32 v57, v114
	v_mfma_f32_16x16x32_f16 v[34:37], v[90:93], v[94:97], v[34:37]
	s_waitcnt vmcnt(7)
	v_cvt_f16_f32_e32 v26, v26
	v_cvt_f16_f32_e32 v29, v29
	v_cvt_pk_f16_f32 v27, v27, v28
	v_cvt_f16_f32_e32 v91, v117
	v_pack_b32_f16 v126, v26, v27
	v_alignbit_b32 v127, v29, v27, 16
	ds_read_b128 v[26:29], v56 offset:13824
	v_cvt_pk_f16_f32 v90, v115, v116
	v_pack_b32_f16 v124, v57, v90
	v_mfma_f32_16x16x32_f16 v[74:77], v[98:101], v[94:97], v[74:77]
	v_alignbit_b32 v125, v91, v90, 16
	s_waitcnt vmcnt(5)
	v_cvt_f16_f32_e32 v130, v30
	v_cvt_pk_f16_f32 v131, v31, v32
	v_cvt_f16_f32_e32 v132, v33
	ds_read_b128 v[90:93], v56 offset:13888
	global_load_dwordx4 v[94:97], v[62:63], off offset:1536
	ds_read_b128 v[98:101], v73 offset:36928
	s_waitcnt lgkmcnt(2)
	v_mfma_f32_16x16x32_f16 v[26:29], v[26:29], v[86:89], v[34:37]
	ds_read_b128 v[30:33], v56 offset:16128
	ds_read_b128 v[102:105], v56 offset:16192
	ds_read_b128 v[106:109], v56 offset:18432
	ds_read_b128 v[110:113], v56 offset:18496
	global_load_dwordx4 v[114:117], v[60:61], off offset:1536
	global_load_dwordx4 v[34:37], v[58:59], off offset:1536
	v_cvt_f16_f32_e32 v57, v22
	v_cvt_pk_f16_f32 v128, v23, v24
	v_cvt_f16_f32_e32 v129, v25
	ds_write2st64_b64 v72, v[118:119], v[120:121] offset1:9
	ds_write2st64_b64 v72, v[122:123], v[124:125] offset0:18 offset1:54
	ds_write_b64 v72, v[126:127] offset:32256
	s_waitcnt lgkmcnt(0)
	s_barrier
	global_load_dwordx4 v[22:25], v[66:67], off offset:1792
	v_mfma_f32_16x16x32_f16 v[74:77], v[30:33], v[86:89], v[74:77]
	global_load_dwordx4 v[30:33], v[64:65], off offset:1792
	v_pack_b32_f16 v118, v57, v128
	v_alignbit_b32 v119, v129, v128, 16
	v_mfma_f32_16x16x32_f16 v[64:67], v[106:109], v[86:89], v[78:81]
	v_pack_b32_f16 v120, v130, v131
	v_alignbit_b32 v121, v132, v131, 16
	s_waitcnt vmcnt(9)
	v_cvt_f16_f32_e32 v38, v38
	v_cvt_f16_f32_e32 v41, v41
	v_cvt_pk_f16_f32 v39, v39, v40
	v_mfma_f32_16x16x32_f16 v[78:81], v[90:93], v[98:101], v[26:29]
	v_pack_b32_f16 v106, v38, v39
	v_alignbit_b32 v107, v41, v39, 16
	s_waitcnt vmcnt(8)
	v_cvt_f16_f32_e32 v38, v42
	v_cvt_f16_f32_e32 v40, v45
	v_cvt_pk_f16_f32 v39, v43, v44
	s_waitcnt vmcnt(7)
	v_cvt_f16_f32_e32 v26, v50
	v_cvt_f16_f32_e32 v27, v53
	v_cvt_pk_f16_f32 v28, v51, v52
	v_mfma_f32_16x16x32_f16 v[50:53], v[102:105], v[98:101], v[74:77]
	v_pack_b32_f16 v102, v26, v28
	v_alignbit_b32 v103, v27, v28, 16
	global_load_dwordx4 v[26:29], v[62:63], off offset:1792
	v_pack_b32_f16 v104, v38, v39
	s_waitcnt vmcnt(7)
	v_cvt_f16_f32_e32 v38, v46
	v_alignbit_b32 v105, v40, v39, 16
	v_cvt_f16_f32_e32 v39, v49
	s_waitcnt vmcnt(6)
	v_cvt_f16_f32_e32 v44, v82
	v_cvt_pk_f16_f32 v40, v47, v48
	v_cvt_pk_f16_f32 v48, v83, v84
	v_pack_b32_f16 v38, v38, v40
	v_alignbit_b32 v39, v39, v40, 16
	ds_read_b128 v[40:43], v56
	v_pack_b32_f16 v108, v44, v48
	v_cvt_f16_f32_e32 v49, v85
	ds_read_b128 v[44:47], v56 offset:2304
	ds_read_b128 v[74:77], v73 offset:27648
	ds_read_b128 v[82:85], v56 offset:4608
	global_load_dwordx4 v[60:63], v[60:61], off offset:1792
	v_mfma_f32_16x16x32_f16 v[64:67], v[110:113], v[98:101], v[64:67]
	ds_read_b128 v[86:89], v56 offset:64
	ds_read_b128 v[90:93], v73 offset:27712
	global_load_dwordx4 v[98:101], v[58:59], off offset:1792
	v_alignbit_b32 v109, v49, v48, 16
	s_waitcnt lgkmcnt(3)
	v_mfma_f32_16x16x32_f16 v[40:43], v[40:43], v[74:77], v[78:81]
	s_waitcnt vmcnt(7)
	v_cvt_pk_f16_f32 v57, v95, v96
	s_nop 0
	ds_read_b128 v[78:81], v56 offset:2368
	v_mfma_f32_16x16x32_f16 v[44:47], v[44:47], v[74:77], v[50:53]
	s_waitcnt vmcnt(6)
	v_cvt_f16_f32_e32 v59, v117
	s_waitcnt vmcnt(5)
	v_cvt_f16_f32_e32 v34, v34
	ds_read_b128 v[48:51], v56 offset:4672
	v_cvt_f16_f32_e32 v52, v94
	v_cvt_f16_f32_e32 v53, v97
	v_cvt_f16_f32_e32 v37, v37
	v_cvt_pk_f16_f32 v35, v35, v36
	s_waitcnt lgkmcnt(4)
	v_mfma_f32_16x16x32_f16 v[64:67], v[82:85], v[74:77], v[64:67]
	v_pack_b32_f16 v52, v52, v57
	v_alignbit_b32 v53, v53, v57, 16
	v_cvt_f16_f32_e32 v57, v114
	s_waitcnt lgkmcnt(2)
	v_mfma_f32_16x16x32_f16 v[40:43], v[86:89], v[90:93], v[40:43]
	ds_write2st64_b64 v72, v[118:119], v[120:121] offset0:27 offset1:36
	ds_write2st64_b64 v72, v[106:107], v[102:103] offset0:45 offset1:72
	ds_write_b64 v72, v[104:105] offset:41472
	v_pack_b32_f16 v86, v34, v35
	v_alignbit_b32 v87, v37, v35, 16
	s_waitcnt lgkmcnt(0)
	s_barrier
	ds_read_b128 v[34:37], v56 offset:13824
	v_cvt_pk_f16_f32 v74, v115, v116
	v_pack_b32_f16 v58, v57, v74
	v_alignbit_b32 v59, v59, v74, 16
	v_mfma_f32_16x16x32_f16 v[48:51], v[48:51], v[90:93], v[64:67]
	s_nop 2
	ds_read_b128 v[64:67], v56 offset:16128
	ds_read_b128 v[74:77], v73 offset:36864
	s_waitcnt vmcnt(4)
	v_cvt_f16_f32_e32 v57, v22
	v_cvt_pk_f16_f32 v89, v23, v24
	v_mfma_f32_16x16x32_f16 v[44:47], v[78:81], v[90:93], v[44:47]
	v_cvt_f16_f32_e32 v90, v25
	ds_read_b128 v[22:25], v56 offset:18432
	ds_read_b128 v[78:81], v56 offset:13888
	ds_read_b128 v[82:85], v73 offset:36928
	s_waitcnt vmcnt(3)
	v_cvt_f16_f32_e32 v30, v30
	s_waitcnt lgkmcnt(3)
	v_mfma_f32_16x16x32_f16 v[34:37], v[34:37], v[74:77], v[40:43]
	v_cvt_f16_f32_e32 v33, v33
	v_cvt_pk_f16_f32 v31, v31, v32
	v_pack_b32_f16 v88, v57, v89
	ds_read_b128 v[40:43], v56 offset:16192
	v_mfma_f32_16x16x32_f16 v[44:47], v[64:67], v[74:77], v[44:47]
	ds_read_b128 v[64:67], v56 offset:18496
	v_alignbit_b32 v89, v90, v89, 16
	v_pack_b32_f16 v90, v30, v31
	s_waitcnt lgkmcnt(4)
	v_mfma_f32_16x16x32_f16 v[22:25], v[22:25], v[74:77], v[48:51]
	v_alignbit_b32 v91, v33, v31, 16
	ds_write2st64_b64 v72, v[38:39], v[108:109] offset1:9
	ds_write2st64_b64 v72, v[52:53], v[58:59] offset0:18 offset1:54
	ds_write_b64 v72, v[86:87] offset:32256
	s_waitcnt lgkmcnt(0)
	v_mfma_f32_16x16x32_f16 v[30:33], v[78:81], v[82:85], v[34:37]
	s_barrier
	s_waitcnt vmcnt(2)
	v_cvt_f16_f32_e32 v57, v26
	ds_read_b128 v[34:37], v56
	v_mfma_f32_16x16x32_f16 v[38:41], v[40:43], v[82:85], v[44:47]
	s_nop 2
	ds_read_b128 v[42:45], v56 offset:2304
	ds_read_b128 v[46:49], v73 offset:27648
	v_cvt_pk_f16_f32 v58, v27, v28
	v_cvt_f16_f32_e32 v59, v29
	v_mfma_f32_16x16x32_f16 v[22:25], v[64:67], v[82:85], v[22:25]
	ds_read_b128 v[50:53], v56 offset:4608
	ds_read_b128 v[64:67], v56 offset:64
	ds_read_b128 v[74:77], v73 offset:27712
	ds_read_b128 v[26:29], v56 offset:2368
	s_waitcnt lgkmcnt(4)
	v_mfma_f32_16x16x32_f16 v[30:33], v[34:37], v[46:49], v[30:33]
	v_mfma_f32_16x16x32_f16 v[34:37], v[42:45], v[46:49], v[38:41]
	s_waitcnt vmcnt(1)
	v_cvt_f16_f32_e32 v44, v60
	v_cvt_f16_f32_e32 v45, v63
	v_pack_b32_f16 v42, v57, v58
	s_waitcnt lgkmcnt(3)
	v_mfma_f32_16x16x32_f16 v[22:25], v[50:53], v[46:49], v[22:25]
	v_cvt_pk_f16_f32 v46, v61, v62
	ds_read_b128 v[38:41], v56 offset:4672
	v_pack_b32_f16 v44, v44, v46
	v_alignbit_b32 v45, v45, v46, 16
	s_waitcnt vmcnt(0)
	v_cvt_f16_f32_e32 v46, v98
	s_waitcnt lgkmcnt(1)
	v_mfma_f32_16x16x32_f16 v[26:29], v[26:29], v[74:77], v[34:37]
	v_alignbit_b32 v43, v59, v58, 16
	ds_write2st64_b64 v72, v[88:89], v[90:91] offset0:27 offset1:36
	ds_write2st64_b64 v72, v[42:43], v[44:45] offset0:45 offset1:72
	v_cvt_f16_f32_e32 v35, v101
	v_cvt_pk_f16_f32 v36, v99, v100
	v_pack_b32_f16 v34, v46, v36
	v_mfma_f32_16x16x32_f16 v[30:33], v[64:67], v[74:77], v[30:33]
	v_alignbit_b32 v35, v35, v36, 16
	ds_write_b64 v72, v[34:35] offset:41472
	s_waitcnt lgkmcnt(0)
	s_barrier
	ds_read_b128 v[34:37], v56 offset:13824
	v_mfma_f32_16x16x32_f16 v[22:25], v[38:41], v[74:77], v[22:25]
	ds_read_b128 v[38:41], v73 offset:36864
	ds_read_b128 v[42:45], v56 offset:13888
	ds_read_b128 v[46:49], v73 offset:36928
	s_waitcnt lgkmcnt(2)
	v_mfma_f32_16x16x32_f16 v[30:33], v[34:37], v[38:41], v[30:33]
	ds_read_b128 v[34:37], v56 offset:16128
	ds_read_b128 v[50:53], v56 offset:16192
	s_waitcnt lgkmcnt(2)
	v_mfma_f32_16x16x32_f16 v[30:33], v[42:45], v[46:49], v[30:33]
	s_waitcnt lgkmcnt(1)
	v_mfma_f32_16x16x32_f16 v[26:29], v[34:37], v[38:41], v[26:29]
	ds_read_b128 v[34:37], v56 offset:18432
	ds_read_b128 v[56:59], v56 offset:18496
	s_waitcnt vmcnt(0)
	s_waitcnt lgkmcnt(0)
	s_nop 2
	v_add_f32_e32 v2, v30, v69
	v_mfma_f32_16x16x32_f16 v[26:29], v[50:53], v[46:49], v[26:29]
	v_cvt_f16_f32_e32 v2, v2
	v_add_f32_e32 v3, v31, v69
	v_cvt_f16_f32_e32 v3, v3
	v_mfma_f32_16x16x32_f16 v[22:25], v[34:37], v[38:41], v[22:25]
	v_add_f32_e32 v4, v32, v69
	v_cvt_f16_f32_e32 v4, v4
	v_add_f32_e32 v5, v33, v69
	v_cvt_f16_f32_e32 v5, v5
	s_barrier
	ds_write_b16 v1, v2
	ds_write_b16 v1, v3 offset:144
	ds_write_b16 v1, v4 offset:288
	ds_write_b16 v1, v5 offset:432
	v_add_f32_e32 v2, v26, v69
	v_mfma_f32_16x16x32_f16 v[22:25], v[56:59], v[46:49], v[22:25]
	v_cvt_f16_f32_e32 v2, v2
	v_add_f32_e32 v3, v27, v69
	v_cvt_f16_f32_e32 v3, v3
	v_add_f32_e32 v4, v28, v69
	v_cvt_f16_f32_e32 v4, v4
	v_add_f32_e32 v5, v29, v69
	v_cvt_f16_f32_e32 v5, v5
	ds_write_b16 v1, v2 offset:2304
	ds_write_b16 v1, v3 offset:2448
	ds_write_b16 v1, v4 offset:2592
	ds_write_b16 v1, v5 offset:2736
	v_add_f32_e32 v2, v22, v69
	v_cvt_f16_f32_e32 v2, v2
	v_add_f32_e32 v3, v23, v69
	v_cvt_f16_f32_e32 v3, v3
	v_add_f32_e32 v4, v24, v69
	v_cvt_f16_f32_e32 v4, v4
	v_add_f32_e32 v5, v25, v69
	v_cvt_f16_f32_e32 v5, v5
	ds_write_b16 v1, v2 offset:4608
	ds_write_b16 v1, v3 offset:4752
	ds_write_b16 v1, v4 offset:4896
	ds_write_b16 v1, v5 offset:5040
	v_and_b32_e32 v2, 7, v0
	v_mul_u32_u24_e32 v10, 12, v2
	v_mul_u32_u24_e32 v2, 0x360, v2
	v_lshrrev_b32_e32 v1, 3, v0
	v_lshlrev_b32_e32 v2, 1, v2
	v_lshl_add_u32 v3, v1, 1, v2
	s_waitcnt lgkmcnt(0)
	s_barrier
	ds_read_u16 v2, v3
	ds_read_u16 v4, v3 offset:144
	ds_read_u16 v5, v3 offset:288
	ds_read_u16 v6, v3 offset:432
	ds_read_u16 v7, v3 offset:576
	ds_read_u16 v8, v3 offset:720
	ds_read_u16 v9, v3 offset:864
	ds_read_u16 v11, v3 offset:1008
	ds_read_u16 v12, v3 offset:1152
	ds_read_u16 v13, v3 offset:1296
	ds_read_u16 v14, v3 offset:1440
	ds_read_u16 v15, v3 offset:1584
	v_lshl_or_b32 v1, s18, 9, v1
	s_waitcnt lgkmcnt(10)
	v_lshl_or_b32 v2, v4, 16, v2
	s_waitcnt lgkmcnt(6)
	v_lshl_or_b32 v4, v8, 16, v7
	v_or_b32_e32 v1, s20, v1
	v_mov_b32_e32 v8, s19
	v_mad_u32_u24 v54, v1, s15, v8
	v_lshl_or_b32 v3, v6, 16, v5
	s_waitcnt lgkmcnt(4)
	v_lshl_or_b32 v5, v11, 16, v9
	v_lshl_add_u64 v[8:9], v[54:55], 1, s[12:13]
	v_lshlrev_b32_e32 v54, 1, v10
	v_lshl_add_u64 v[8:9], v[8:9], 0, v[54:55]
	s_waitcnt lgkmcnt(2)
	v_lshl_or_b32 v6, v13, 16, v12
	s_waitcnt lgkmcnt(0)
	v_lshl_or_b32 v7, v15, 16, v14
	global_store_dwordx4 v[8:9], v[2:5], off
	global_store_dwordx2 v[8:9], v[6:7], off offset:16
	s_mov_b64 s[12:13], 0
